# bundle9 + QKV GEMM phase entry staggered by workgroup class ((blk>>3)&3 x ~5us) to de-synchronise epilogue store bursts
# baseline (speedup 1.0000x reference)
.LBB0_252:
	v_readlane_b32 s98, v254, 13
	s_nop 3
	s_bfe_u32 s98, s98, 0x20006
	s_cmp_eq_u32 s98, 0
	s_cbranch_scc1 .Lgstag_q_done
.Lgstag_q_loop:
	s_sleep 127
	s_sleep 60
	s_add_i32 s98, s98, -1
	s_cmp_lg_u32 s98, 0
	s_cbranch_scc1 .Lgstag_q_loop
